# helper share raised to 10x171 runs now that the attention loops no longer drain their prefetch (computing workgroups finish earlier)
# speedup vs baseline: 1.0159x; 1.0132x over previous
; #define LDS_AS __attribute__((address_space(3)))
; #define OPAQUE_TID(P) (((P).wid0 << 6) | lane_id_now())
; template <int NS, bool STREAM_ONLY = false>
; DI void convert_experts_dma(const Params& p, LDS_AS unsigned char* lds, int bid, int nb) {
;   const int tid = OPAQUE_TID(p), wid = __builtin_amdgcn_readfirstlane(tid >> 6), lane = tid & 63;
;   constexpr int NT = 32 * 1536;
;   const int nvalid = bid < NT / CVG ? CVG * ((NT / CVG - bid + nb - 1) / nb) : 0;
;     ...
;   const __amdgpu_buffer_rsrc_t rs1 = __builtin_amdgcn_make_buffer_rsrc((void*)p.w_gate_up, 0, 0x40000000u, 0x00020000);
;   const __amdgpu_buffer_rsrc_t rs2 = __builtin_amdgcn_make_buffer_rsrc((void*)p.w_down, 0, 0x20000000u, 0x00020000);
;   const __amdgpu_buffer_rsrc_t rs0 = __builtin_amdgcn_make_buffer_rsrc((void*)p.w_down, 0, 0u, 0x00020000);
;   const unsigned vo1 = ((unsigned)lane >> 4) * 16384u + ((((unsigned)lane & 15u) ^ (unsigned)wid) << 4);
;   const unsigned vo2 = ((unsigned)lane >> 4) * 8192u + ((((unsigned)lane & 15u) ^ (unsigned)wid) << 4);
;   const unsigned ldsw = (unsigned)__builtin_amdgcn_readfirstlane((int)(unsigned)(size_t)lds) + (unsigned)wid * 4096u;
;   const int n = 8 * wid + (lane >> 3), kc = lane & 7;
;   const unsigned roff = (unsigned)kc * 4096u + ((((unsigned)n >> 2) ^ (unsigned)kc) << 4) + (((unsigned)n & 3u) << 2);
.LBB0_1119:
	s_or_b64 exec, exec, s[0:1]
	s_mov_b64 s[12:13], 0
	s_mov_b32 s20, 0
	s_mov_b64 s[0:1], 0
	v_readlane_b32 s97, v255, 13
	s_mov_b32 s99, s96
	s_nop 0
	s_mov_b32 s98, s97
	s_cmp_lg_u32 s55, 0
	s_cbranch_scc0 .LBB0_1181
	v_readlane_b32 s98, v255, 17
	s_sub_i32 s99, s96, s55
	s_add_i32 s98, s98, 0x2952
	s_branch .LBB0_1181
.LBB0_1121:
	v_mov_b32_e32 v0, 0
	ds_read_b32 v2, v0
	ds_read_b32 v3, v0 offset:4
	s_waitcnt lgkmcnt(0)
	s_barrier
	v_mbcnt_lo_u32_b32 v0, -1, 0
	v_mbcnt_hi_u32_b32 v0, -1, v0
	s_mov_b32 s6, 0
	v_or_b32_e32 v1, s87, v0
	s_cmpk_gt_i32 s54, 0x2951
	v_readfirstlane_b32 s0, v1
	s_mov_b32 s18, 0
	s_cbranch_scc1 .LBB0_1123
	s_abs_i32 s1, s55
	v_cvt_f32_u32_e32 v1, s1
	s_sub_i32 s2, s55, s54
	s_add_i32 s3, s2, 0x2951
	s_sub_i32 s2, 0xffffd6af, s2
	v_rcp_iflag_f32_e32 v1, v1
	s_xor_b32 s5, s3, s55
	s_sub_i32 s4, 0, s1
	s_max_i32 s2, s3, s2
	v_mul_f32_e32 v1, 0x4f7ffffe, v1
	v_cvt_u32_f32_e32 v1, v1
	s_ashr_i32 s3, s5, 31
	v_readfirstlane_b32 s5, v1
	s_mul_i32 s4, s4, s5
	s_mul_hi_u32 s4, s5, s4
	s_add_i32 s5, s5, s4
	s_mul_hi_u32 s4, s2, s5
	s_mul_i32 s5, s4, s1
	s_sub_i32 s2, s2, s5
	s_add_i32 s7, s4, 1
	s_sub_i32 s5, s2, s1
	s_cmp_ge_u32 s2, s1
	s_cselect_b32 s4, s7, s4
	s_cselect_b32 s2, s5, s2
	s_add_i32 s5, s4, 1
	s_cmp_ge_u32 s2, s1
	s_cselect_b32 s1, s5, s4
	s_xor_b32 s1, s1, s3
	s_sub_i32 s1, s1, s3
	s_lshl_b32 s18, s1, 2
